# three serialized load-wait loops given 4-8 loads in flight: prologue weight-scale sums, prologue silu LDS fill, norm2 router-weight LDS fill (same arithmetic order)
# speedup vs baseline: 1.0083x; 1.0083x over previous
; #define LAS __attribute__((address_space(3)))
; __device__ __forceinline__ float silu_f(float x) { return x / (1.f + __expf(-x)); }
; __device__ __forceinline__ void phase_prologue(const Params& p, const Ctx& F) {
;     for (int item = F.bid; item < 192; item += F.G) {
;         LAS float* sl = (LAS float*)F.lds; LAS float* red = (LAS float*)(F.lds + 73728);
;         for (int i = F.tid; i < 9 * DM; i += NTHR) { const int r = i >> 11, d = i & 2047; const float v = r < 8 ? p.c[r * DM + d] : p.c_ctx[d]; sl[i] = silu_f(v); }
;         __syncthreads();
.LBB0_9:
	s_and_saveexec_b64 s[14:15], s[0:1]
	s_cbranch_execz .LBB0_12
	v_mov_b64_e32 v[12:13], v[8:9]
	v_mov_b32_e32 v14, v42
	v_mov_b32_e32 v15, v2
	s_mov_b32 s16, 9
.Lsilu_loop:
	v_and_b32_e32 v4, 0x7ff, v15
	v_lshlrev_b32_e32 v4, 2, v4
	v_lshl_add_u64 v[16:17], s[70:71], 0, v[4:5]
	v_cmp_gt_i32_e32 vcc, s21, v15
	s_nop 1
	v_cndmask_b32_e32 v17, v17, v13, vcc
	v_cndmask_b32_e32 v16, v16, v12, vcc
	global_load_dword v44, v[16:17], off
	v_add_u32_e32 v15, 0x200, v15
	v_lshl_add_u64 v[12:13], v[12:13], 0, s[10:11]
	v_and_b32_e32 v4, 0x7ff, v15
	v_lshlrev_b32_e32 v4, 2, v4
	v_lshl_add_u64 v[16:17], s[70:71], 0, v[4:5]
	v_cmp_gt_i32_e32 vcc, s21, v15
	s_nop 1
	v_cndmask_b32_e32 v17, v17, v13, vcc
	v_cndmask_b32_e32 v16, v16, v12, vcc
	global_load_dword v45, v[16:17], off
	v_add_u32_e32 v15, 0x200, v15
	v_lshl_add_u64 v[12:13], v[12:13], 0, s[10:11]
	v_and_b32_e32 v4, 0x7ff, v15
	v_lshlrev_b32_e32 v4, 2, v4
	v_lshl_add_u64 v[16:17], s[70:71], 0, v[4:5]
	v_cmp_gt_i32_e32 vcc, s21, v15
	s_nop 1
	v_cndmask_b32_e32 v17, v17, v13, vcc
	v_cndmask_b32_e32 v16, v16, v12, vcc
	global_load_dword v46, v[16:17], off
	v_add_u32_e32 v15, 0x200, v15
	v_lshl_add_u64 v[12:13], v[12:13], 0, s[10:11]
	v_and_b32_e32 v4, 0x7ff, v15
	v_lshlrev_b32_e32 v4, 2, v4
	v_lshl_add_u64 v[16:17], s[70:71], 0, v[4:5]
	v_cmp_gt_i32_e32 vcc, s21, v15
	s_nop 1
	v_cndmask_b32_e32 v17, v17, v13, vcc
	v_cndmask_b32_e32 v16, v16, v12, vcc
	global_load_dword v47, v[16:17], off
	v_add_u32_e32 v15, 0x200, v15
	v_lshl_add_u64 v[12:13], v[12:13], 0, s[10:11]
	s_waitcnt vmcnt(3)
	v_mov_b32_e32 v4, v44
	v_mul_f32_e32 v16, 0xbfb8aa3b, v4
	v_exp_f32_e32 v16, v16
	s_nop 0
	v_add_f32_e32 v16, 1.0, v16
	v_div_scale_f32 v17, s[34:35], v16, v16, v4
	v_rcp_f32_e32 v18, v17
	v_div_scale_f32 v19, vcc, v4, v16, v4
	v_fma_f32 v20, -v17, v18, 1.0
	v_fmac_f32_e32 v18, v20, v18
	v_mul_f32_e32 v20, v19, v18
	v_fma_f32 v21, -v17, v20, v19
	v_fmac_f32_e32 v20, v21, v18
	v_fma_f32 v17, -v17, v20, v19
	v_div_fmas_f32 v17, v17, v18, v20
	v_div_fixup_f32 v4, v17, v16, v4
	ds_write_b32 v14, v4
	v_add_u32_e32 v14, 0x800, v14
	s_waitcnt vmcnt(2)
	v_mov_b32_e32 v4, v45
	v_mul_f32_e32 v16, 0xbfb8aa3b, v4
	v_exp_f32_e32 v16, v16
	s_nop 0
	v_add_f32_e32 v16, 1.0, v16
	v_div_scale_f32 v17, s[34:35], v16, v16, v4
	v_rcp_f32_e32 v18, v17
	v_div_scale_f32 v19, vcc, v4, v16, v4
	v_fma_f32 v20, -v17, v18, 1.0
	v_fmac_f32_e32 v18, v20, v18
	v_mul_f32_e32 v20, v19, v18
	v_fma_f32 v21, -v17, v20, v19
	v_fmac_f32_e32 v20, v21, v18
	v_fma_f32 v17, -v17, v20, v19
	v_div_fmas_f32 v17, v17, v18, v20
	v_div_fixup_f32 v4, v17, v16, v4
	ds_write_b32 v14, v4
	v_add_u32_e32 v14, 0x800, v14
	s_waitcnt vmcnt(1)
	v_mov_b32_e32 v4, v46
	v_mul_f32_e32 v16, 0xbfb8aa3b, v4
	v_exp_f32_e32 v16, v16
	s_nop 0
	v_add_f32_e32 v16, 1.0, v16
	v_div_scale_f32 v17, s[34:35], v16, v16, v4
	v_rcp_f32_e32 v18, v17
	v_div_scale_f32 v19, vcc, v4, v16, v4
	v_fma_f32 v20, -v17, v18, 1.0
	v_fmac_f32_e32 v18, v20, v18
	v_mul_f32_e32 v20, v19, v18
	v_fma_f32 v21, -v17, v20, v19
	v_fmac_f32_e32 v20, v21, v18
	v_fma_f32 v17, -v17, v20, v19
	v_div_fmas_f32 v17, v17, v18, v20
	v_div_fixup_f32 v4, v17, v16, v4
	ds_write_b32 v14, v4
	v_add_u32_e32 v14, 0x800, v14
	s_waitcnt vmcnt(0)
	v_mov_b32_e32 v4, v47
	v_mul_f32_e32 v16, 0xbfb8aa3b, v4
	v_exp_f32_e32 v16, v16
	s_nop 0
	v_add_f32_e32 v16, 1.0, v16
	v_div_scale_f32 v17, s[34:35], v16, v16, v4
	v_rcp_f32_e32 v18, v17
	v_div_scale_f32 v19, vcc, v4, v16, v4
	v_fma_f32 v20, -v17, v18, 1.0
	v_fmac_f32_e32 v18, v20, v18
	v_mul_f32_e32 v20, v19, v18
	v_fma_f32 v21, -v17, v20, v19
	v_fmac_f32_e32 v20, v21, v18
	v_fma_f32 v17, -v17, v20, v19
	v_div_fmas_f32 v17, v17, v18, v20
	v_div_fixup_f32 v4, v17, v16, v4
	ds_write_b32 v14, v4
	v_add_u32_e32 v14, 0x800, v14
	s_sub_u32 s16, s16, 1
	s_cmp_lg_u32 s16, 0
	s_cbranch_scc1 .Lsilu_loop

; __device__ __forceinline__ void phase_prologue(const Params& p, const Ctx& F) {
;     ...
;         float ss = 0.f;
;         for (int i = F.tid; i < 8 * N; i += NTHR) { const float v = W[i]; ss += v * v; }
.LBB0_33:
	v_lshl_add_u64 v[6:7], s[6:7], 0, v[4:5]
	v_mov_b32_e32 v3, 0
	s_lshr_b32 s6, s9, 12
.Lsc_loop:
	global_load_dword v16, v[6:7], off
	v_lshl_add_u64 v[6:7], v[6:7], 0, s[12:13]
	global_load_dword v17, v[6:7], off
	v_lshl_add_u64 v[6:7], v[6:7], 0, s[12:13]
	global_load_dword v18, v[6:7], off
	v_lshl_add_u64 v[6:7], v[6:7], 0, s[12:13]
	global_load_dword v19, v[6:7], off
	v_lshl_add_u64 v[6:7], v[6:7], 0, s[12:13]
	global_load_dword v20, v[6:7], off
	v_lshl_add_u64 v[6:7], v[6:7], 0, s[12:13]
	global_load_dword v21, v[6:7], off
	v_lshl_add_u64 v[6:7], v[6:7], 0, s[12:13]
	global_load_dword v22, v[6:7], off
	v_lshl_add_u64 v[6:7], v[6:7], 0, s[12:13]
	global_load_dword v23, v[6:7], off
	v_lshl_add_u64 v[6:7], v[6:7], 0, s[12:13]
	s_waitcnt vmcnt(7)
	v_fmac_f32_e32 v3, v16, v16
	s_waitcnt vmcnt(6)
	v_fmac_f32_e32 v3, v17, v17
	s_waitcnt vmcnt(5)
	v_fmac_f32_e32 v3, v18, v18
	s_waitcnt vmcnt(4)
	v_fmac_f32_e32 v3, v19, v19
	s_waitcnt vmcnt(3)
	v_fmac_f32_e32 v3, v20, v20
	s_waitcnt vmcnt(2)
	v_fmac_f32_e32 v3, v21, v21
	s_waitcnt vmcnt(1)
	v_fmac_f32_e32 v3, v22, v22
	s_waitcnt vmcnt(0)
	v_fmac_f32_e32 v3, v23, v23
	s_sub_u32 s6, s6, 1
	s_cmp_lg_u32 s6, 0
	s_cbranch_scc1 .Lsc_loop

; #define LAS __attribute__((address_space(3)))
; __device__ __forceinline__ void phase_norm2(const Params& p, const Ctx& F, const int l) {
;     LAS float* wr = (LAS float*)F.lds;
;     for (int i = F.tid; i < DM * NEXP; i += NTHR) { const int d = i >> 4, e = i & 15; wr[e * DM + d] = p.w_router[(size_t)l * DM * NEXP + i]; }
;     __syncthreads();
.LBB0_893:
	s_andn2_b64 vcc, exec, s[0:1]
	s_cbranch_vccnz .LBB0_1001
	v_readlane_b32 s2, v252, 35
	v_mov_b32_e32 v2, v0
	s_mov_b64 s[0:1], s[90:91]
	v_readlane_b32 s13, v252, 0
	v_readlane_b32 s3, v252, 36
	s_load_dword s16, s[2:3], 0x0
	v_readfirstlane_b32 s12, v2
	v_cmp_gt_i32_e32 vcc, s87, v2
	s_and_saveexec_b64 s[2:3], vcc
	s_cbranch_execz .LBB0_907
	v_readlane_b32 s36, v252, 17
	v_readlane_b32 s42, v252, 23
	v_readlane_b32 s43, v252, 24
	s_lshl_b32 s60, s78, 15
	s_lshl_b64 s[6:7], s[60:61], 2
	s_add_u32 s6, s42, s6
	s_addc_u32 s7, s43, s7
	v_readlane_b32 s37, v252, 18
	v_readlane_b32 s38, v252, 19
	v_readlane_b32 s39, v252, 20
	v_readlane_b32 s40, v252, 21
	v_readlane_b32 s41, v252, 22
	v_readlane_b32 s44, v252, 25
	v_readlane_b32 s45, v252, 26
	v_readlane_b32 s46, v252, 27
	v_readlane_b32 s47, v252, 28
	v_readlane_b32 s48, v252, 29
	v_readlane_b32 s49, v252, 30
	v_readlane_b32 s50, v252, 31
	v_readlane_b32 s51, v252, 32
	v_lshlrev_b32_e32 v1, 2, v2
	v_and_b32_e32 v3, 15, v2
	v_lshlrev_b32_e32 v3, 13, v3
	v_lshrrev_b32_e32 v4, 4, v2
	v_lshl_add_u32 v3, v4, 2, v3
	s_mov_b32 s8, 8
.Lrf_loop:
	global_load_dword v16, v1, s[6:7]
	v_add_u32_e32 v1, 0x800, v1
	global_load_dword v17, v1, s[6:7]
	v_add_u32_e32 v1, 0x800, v1
	global_load_dword v18, v1, s[6:7]
	v_add_u32_e32 v1, 0x800, v1
	global_load_dword v19, v1, s[6:7]
	v_add_u32_e32 v1, 0x800, v1
	global_load_dword v20, v1, s[6:7]
	v_add_u32_e32 v1, 0x800, v1
	global_load_dword v21, v1, s[6:7]
	v_add_u32_e32 v1, 0x800, v1
	global_load_dword v22, v1, s[6:7]
	v_add_u32_e32 v1, 0x800, v1
	global_load_dword v23, v1, s[6:7]
	v_add_u32_e32 v1, 0x800, v1
	s_waitcnt vmcnt(7)
	ds_write_b32 v3, v16 offset:0
	s_waitcnt vmcnt(6)
	ds_write_b32 v3, v17 offset:128
	s_waitcnt vmcnt(5)
	ds_write_b32 v3, v18 offset:256
	s_waitcnt vmcnt(4)
	ds_write_b32 v3, v19 offset:384
	s_waitcnt vmcnt(3)
	ds_write_b32 v3, v20 offset:512
	s_waitcnt vmcnt(2)
	ds_write_b32 v3, v21 offset:640
	s_waitcnt vmcnt(1)
	ds_write_b32 v3, v22 offset:768
	s_waitcnt vmcnt(0)
	ds_write_b32 v3, v23 offset:896
	v_add_u32_e32 v3, 0x400, v3
	s_sub_u32 s8, s8, 1
	s_cmp_lg_u32 s8, 0
	s_cbranch_scc1 .Lrf_loop
